# speedup vs baseline: 1.0401x; 1.0058x over previous
_Z5k_midPK15HIP_vector_typeIjLj2EEPKiPiPfPjPDF16_:
	s_load_dwordx2 s[4:5], s[0:1], 0x8
	s_load_dwordx2 s[44:45], s[0:1], 0x28
	s_and_b32 s3, s2, 7
	s_lshr_b32 s2, s2, 3
	s_mul_i32 s35, s3, 49
	s_add_i32 s35, s35, s2
	v_min_u32_e32 v1, 0x186, v0
	s_movk_i32 s2, 0x188
	v_mov_b32_e32 v2, s35
	v_mad_u32_u24 v4, v1, s2, v2
	v_mov_b32_e32 v5, 0
	s_waitcnt lgkmcnt(0)
	v_lshl_add_u64 v[2:3], v[4:5], 2, s[4:5]
	global_load_dwordx2 v[2:3], v[2:3], off
	s_lshl_b32 s46, s35, 8
	v_lshrrev_b32_e32 v72, 3, v0
	v_or_b32_e32 v72, s46, v72
	v_and_b32_e32 v56, 7, v0
	v_lshlrev_b32_e32 v56, 4, v56
	v_min_u32_e32 v60, 0x1869f, v72
	v_lshl_or_b32 v60, v60, 7, v56
	v_add_u32_e32 v64, 64, v72
	v_min_u32_e32 v64, 0x1869f, v64
	v_lshl_or_b32 v64, v64, 7, v56
	v_add_u32_e32 v68, 0x80, v72
	v_min_u32_e32 v68, 0x1869f, v68
	v_lshl_or_b32 v68, v68, 7, v56
	v_add_u32_e32 v72, 0xc0, v72
	v_min_u32_e32 v72, 0x1869f, v72
	v_lshl_or_b32 v72, v72, 7, v56
	global_load_dwordx4 v[60:63], v60, s[44:45]
	global_load_dwordx4 v[64:67], v64, s[44:45]
	global_load_dwordx4 v[68:71], v68, s[44:45]
	global_load_dwordx4 v[56:59], v72, s[44:45]
	s_movk_i32 s2, 0x100
	v_cmp_gt_u32_e64 s[4:5], s2, v0
	v_lshlrev_b32_e32 v1, 2, v0
	s_and_saveexec_b64 s[2:3], s[4:5]
	ds_write_b32 v1, v5 offset:3132
	s_or_b64 exec, exec, s[2:3]
	ds_write_b32 v1, v5 offset:5248
	s_mov_b32 s50, 0xc34f
	s_movk_i32 s2, 0x187
	v_cmp_gt_u32_e32 vcc, s2, v0
	s_waitcnt vmcnt(4)
	v_sub_u32_e32 v3, v3, v2
	v_and_b32_e32 v7, 63, v0
	v_cndmask_b32_e32 v6, 0, v2, vcc
	v_cndmask_b32_e32 v4, 0, v3, vcc
	v_lshrrev_b32_e32 v20, 6, v0
	v_add_u32_dpp v6, v6, v6 row_shr:1 row_mask:0xf bank_mask:0xf bound_ctrl:1
	v_add_u32_dpp v4, v4, v4 row_shr:1 row_mask:0xf bank_mask:0xf bound_ctrl:1
	v_cmp_eq_u32_e64 s[6:7], 63, v7
	v_add_u32_dpp v6, v6, v6 row_shr:2 row_mask:0xf bank_mask:0xf bound_ctrl:1
	v_add_u32_dpp v4, v4, v4 row_shr:2 row_mask:0xf bank_mask:0xf bound_ctrl:1
	s_nop 0
	v_add_u32_dpp v6, v6, v6 row_shr:4 row_mask:0xf bank_mask:0xf bound_ctrl:1
	v_add_u32_dpp v4, v4, v4 row_shr:4 row_mask:0xf bank_mask:0xf bound_ctrl:1
	s_nop 0
	v_add_u32_dpp v6, v6, v6 row_shr:8 row_mask:0xf bank_mask:0xf bound_ctrl:1
	v_add_u32_dpp v4, v4, v4 row_shr:8 row_mask:0xf bank_mask:0xf bound_ctrl:1
	s_nop 0
	v_add_u32_dpp v6, v6, v6 row_bcast:15 row_mask:0xa bank_mask:0xf
	v_add_u32_dpp v4, v4, v4 row_bcast:15 row_mask:0xa bank_mask:0xf
	s_nop 0
	v_mov_b32_dpp v5, v6 row_bcast:31 row_mask:0xc bank_mask:0xf
	v_add_u32_dpp v4, v4, v4 row_bcast:31 row_mask:0xc bank_mask:0xf
	s_and_saveexec_b64 s[2:3], s[6:7]
	v_add_u32_e32 v5, v6, v5
	v_lshlrev_b32_e32 v6, 2, v20
	v_add_u32_e32 v6, 0x1000, v6
	ds_write2_b32 v6, v4, v5 offset0:15 offset1:23
	s_or_b64 exec, exec, s[2:3]
	v_mov_b32_e32 v5, 0x1074
	s_waitcnt lgkmcnt(0)
	s_barrier
	ds_read2_b32 v[6:7], v5 offset1:1
	v_mov_b32_e32 v5, 0x106c
	v_mov_b32_e32 v10, 0x1064
	v_mov_b32_e32 v12, 0x105c
	ds_read2_b32 v[8:9], v5 offset1:1
	ds_read2_b32 v[10:11], v10 offset1:1
	ds_read2_b32 v[12:13], v12 offset1:1
	v_mov_b32_e32 v5, 0x1054
	s_waitcnt lgkmcnt(3)
	v_readfirstlane_b32 s36, v7
	v_readfirstlane_b32 s38, v6
	s_waitcnt lgkmcnt(1)
	v_readfirstlane_b32 s42, v10
	s_waitcnt lgkmcnt(0)
	v_readfirstlane_b32 s43, v12
	ds_read2_b32 v[6:7], v5 offset1:1
	v_mov_b32_e32 v5, 0x104c
	v_mov_b32_e32 v10, 0x1044
	v_mov_b32_e32 v12, 0x103c
	v_readfirstlane_b32 s39, v9
	v_readfirstlane_b32 s40, v8
	v_readfirstlane_b32 s41, v11
	v_readfirstlane_b32 s37, v13
	ds_read2_b32 v[8:9], v5 offset1:1
	ds_read2_b32 v[10:11], v10 offset1:1
	ds_read2_b32 v[12:13], v12 offset1:1
	s_waitcnt lgkmcnt(3)
	v_readfirstlane_b32 s10, v7
	v_readfirstlane_b32 s11, v6
	s_waitcnt lgkmcnt(2)
	v_readfirstlane_b32 s12, v9
	v_readfirstlane_b32 s13, v8
	s_waitcnt lgkmcnt(1)
	v_readfirstlane_b32 s14, v11
	v_readfirstlane_b32 s15, v10
	s_waitcnt lgkmcnt(0)
	v_readfirstlane_b32 s16, v13
	v_readfirstlane_b32 s17, v12
	s_and_saveexec_b64 s[2:3], vcc
	s_cbranch_execz .LBB1_6
	s_movk_i32 s8, 0x17f
	v_mov_b32_e32 v5, s12
	v_cmp_lt_u32_e32 vcc, s8, v0
	s_movk_i32 s8, 0x13f
	v_mov_b32_e32 v6, s13
	v_cndmask_b32_e32 v5, 0, v5, vcc
	v_cmp_lt_u32_e32 vcc, s8, v0
	s_movk_i32 s8, 0xff
	v_mov_b32_e32 v7, s14
	v_cndmask_b32_e32 v6, 0, v6, vcc
	v_cmp_lt_u32_e32 vcc, s8, v0
	s_movk_i32 s8, 0xbf
	v_mov_b32_e32 v8, s15
	v_cndmask_b32_e32 v7, 0, v7, vcc
	v_cmp_lt_u32_e32 vcc, s8, v0
	s_movk_i32 s8, 0x7f
	v_mov_b32_e32 v9, s16
	v_cndmask_b32_e32 v8, 0, v8, vcc
	v_cmp_lt_u32_e32 vcc, s8, v0
	v_mov_b32_e32 v10, s17
	v_sub_u32_e32 v3, v4, v3
	v_cndmask_b32_e32 v9, 0, v9, vcc
	v_cmp_lt_u32_e32 vcc, 63, v0
	v_lshl_add_u32 v2, v0, 12, v2
	s_nop 0
	v_cndmask_b32_e32 v10, 0, v10, vcc
	v_add3_u32 v3, v3, v10, v9
	v_add3_u32 v3, v3, v8, v7
	v_add3_u32 v3, v3, v6, v5
	ds_write_b32 v1, v3
	ds_write_b32 v1, v2 offset:1568

.Lmid_fill_done:
	s_mov_b64 exec, s[12:13]
	s_waitcnt lgkmcnt(0)
	s_barrier
	v_min_u32_e32 v30, s10, v0
	v_min_u32_e32 v31, s10, v23
	v_min_u32_e32 v32, s10, v28
	v_min_u32_e32 v33, s10, v22
	v_min_u32_e32 v34, s10, v27
	v_min_u32_e32 v35, s10, v26
	v_min_u32_e32 v36, s10, v25
	v_min_u32_e32 v37, s10, v24
	v_min_u32_e32 v38, s10, v21
	v_lshlrev_b32_e32 v30, 2, v30
	v_lshlrev_b32_e32 v31, 2, v31
	v_lshlrev_b32_e32 v32, 2, v32
	v_lshlrev_b32_e32 v33, 2, v33
	v_lshlrev_b32_e32 v34, 2, v34
	v_lshlrev_b32_e32 v35, 2, v35
	v_lshlrev_b32_e32 v36, 2, v36
	v_lshlrev_b32_e32 v37, 2, v37
	v_lshlrev_b32_e32 v38, 2, v38
	ds_read_b32 v30, v30 offset:8192
	ds_read_b32 v31, v31 offset:8192
	ds_read_b32 v32, v32 offset:8192
	ds_read_b32 v33, v33 offset:8192
	ds_read_b32 v34, v34 offset:8192
	ds_read_b32 v35, v35 offset:8192
	ds_read_b32 v36, v36 offset:8192
	ds_read_b32 v37, v37 offset:8192
	ds_read_b32 v38, v38 offset:8192
	s_cmp_gt_i32 s33, 0
	s_cselect_b64 vcc, -1, 0
	s_waitcnt lgkmcnt(8)
	v_lshlrev_b32_e32 v30, 3, v30
	v_cndmask_b32_e32 v30, 0, v30, vcc
	global_load_dwordx2 v[18:19], v30, s[8:9]
	s_waitcnt lgkmcnt(7)
	v_lshlrev_b32_e32 v31, 3, v31
	v_cndmask_b32_e32 v31, 0, v31, vcc
	global_load_dwordx2 v[16:17], v31, s[8:9]
	s_waitcnt lgkmcnt(6)
	v_lshlrev_b32_e32 v32, 3, v32
	v_cndmask_b32_e32 v32, 0, v32, vcc
	global_load_dwordx2 v[12:13], v32, s[8:9]
	s_waitcnt lgkmcnt(5)
	v_lshlrev_b32_e32 v33, 3, v33
	v_cndmask_b32_e32 v33, 0, v33, vcc
	global_load_dwordx2 v[8:9], v33, s[8:9]
	s_waitcnt lgkmcnt(4)
	v_lshlrev_b32_e32 v34, 3, v34
	v_cndmask_b32_e32 v34, 0, v34, vcc
	global_load_dwordx2 v[14:15], v34, s[8:9]
	s_waitcnt lgkmcnt(3)
	v_lshlrev_b32_e32 v35, 3, v35
	v_cndmask_b32_e32 v35, 0, v35, vcc
	global_load_dwordx2 v[10:11], v35, s[8:9]
	s_waitcnt lgkmcnt(2)
	v_lshlrev_b32_e32 v36, 3, v36
	v_cndmask_b32_e32 v36, 0, v36, vcc
	global_load_dwordx2 v[6:7], v36, s[8:9]
	s_waitcnt lgkmcnt(1)
	v_lshlrev_b32_e32 v37, 3, v37
	v_cndmask_b32_e32 v37, 0, v37, vcc
	global_load_dwordx2 v[4:5], v37, s[8:9]
	s_waitcnt lgkmcnt(0)
	v_lshlrev_b32_e32 v38, 3, v38
	v_cndmask_b32_e32 v38, 0, v38, vcc
	global_load_dwordx2 v[2:3], v38, s[8:9]
	v_mov_b32_e32 v29, 0
	v_cmp_gt_i32_e32 vcc, s33, v0
	v_mov_b32_e32 v34, 0
	s_waitcnt vmcnt(8)
	v_lshrrev_b32_e32 v31, 14, v18
	v_and_b32_e32 v73, 0x1ffff, v18
	v_and_b32_e32 v31, 0x7f8, v31
	v_cmp_lt_u32_e64 s[48:49], s50, v73
	s_nop 1
	v_cndmask_b32_e64 v73, 0, 4, s[48:49]
	v_or_b32_e32 v31, v31, v73
	s_and_saveexec_b64 s[8:9], vcc
	v_and_b32_e32 v30, 0x1fffc, v31
	v_mov_b32_e32 v32, 1
	ds_add_rtn_u32 v34, v30, v32 offset:5248
	s_or_b64 exec, exec, s[8:9]
	v_cmp_gt_i32_e64 s[8:9], s33, v23
	s_waitcnt vmcnt(7)
	v_lshrrev_b32_e32 v30, 14, v16
	v_and_b32_e32 v73, 0x1ffff, v16
	v_and_b32_e32 v30, 0x7f8, v30
	v_cmp_lt_u32_e64 s[48:49], s50, v73
	s_nop 1
	v_cndmask_b32_e64 v73, 0, 4, s[48:49]
	v_or_b32_e32 v30, v30, v73
	s_and_saveexec_b64 s[10:11], s[8:9]
	v_and_b32_e32 v29, 0x1fffc, v30
	v_mov_b32_e32 v32, 1
	ds_add_rtn_u32 v29, v29, v32 offset:5248
	s_or_b64 exec, exec, s[10:11]
	v_cmp_gt_i32_e64 s[10:11], s33, v28
	v_mov_b32_e32 v28, 0
	s_waitcnt vmcnt(6)
	v_lshrrev_b32_e32 v33, 14, v12
	v_and_b32_e32 v73, 0x1ffff, v12
	v_and_b32_e32 v33, 0x7f8, v33
	v_cmp_lt_u32_e64 s[48:49], s50, v73
	s_nop 1
	v_cndmask_b32_e64 v73, 0, 4, s[48:49]
	v_or_b32_e32 v33, v33, v73
	v_mov_b32_e32 v36, 0
	s_and_saveexec_b64 s[12:13], s[10:11]
	v_and_b32_e32 v32, 0x1fffc, v33
	v_mov_b32_e32 v35, 1
	ds_add_rtn_u32 v36, v32, v35 offset:5248
	s_or_b64 exec, exec, s[12:13]
	v_cmp_gt_i32_e64 s[12:13], s33, v22
	s_waitcnt vmcnt(5)
	v_lshrrev_b32_e32 v32, 14, v8
	v_and_b32_e32 v73, 0x1ffff, v8
	v_and_b32_e32 v32, 0x7f8, v32
	v_cmp_lt_u32_e64 s[48:49], s50, v73
	s_nop 1
	v_cndmask_b32_e64 v73, 0, 4, s[48:49]
	v_or_b32_e32 v32, v32, v73
	s_and_saveexec_b64 s[14:15], s[12:13]
	v_and_b32_e32 v28, 0x1fffc, v32
	v_mov_b32_e32 v35, 1
	ds_add_rtn_u32 v28, v28, v35 offset:5248
	s_or_b64 exec, exec, s[14:15]
	v_cmp_gt_i32_e64 s[14:15], s33, v27
	v_mov_b32_e32 v27, 0
	s_waitcnt vmcnt(4)
	v_lshrrev_b32_e32 v35, 14, v14
	v_and_b32_e32 v73, 0x1ffff, v14
	v_and_b32_e32 v35, 0x7f8, v35
	v_cmp_lt_u32_e64 s[48:49], s50, v73
	s_nop 1
	v_cndmask_b32_e64 v73, 0, 4, s[48:49]
	v_or_b32_e32 v35, v35, v73
	v_mov_b32_e32 v38, 0
	s_and_saveexec_b64 s[16:17], s[14:15]
	v_and_b32_e32 v37, 0x1fffc, v35
	v_mov_b32_e32 v38, 1
	ds_add_rtn_u32 v38, v37, v38 offset:5248
	s_or_b64 exec, exec, s[16:17]
	v_cmp_gt_i32_e64 s[16:17], s33, v26
	s_waitcnt vmcnt(3)
	v_lshrrev_b32_e32 v26, 14, v10
	v_and_b32_e32 v73, 0x1ffff, v10
	v_and_b32_e32 v26, 0x7f8, v26
	v_cmp_lt_u32_e64 s[48:49], s50, v73
	s_nop 1
	v_cndmask_b32_e64 v73, 0, 4, s[48:49]
	v_or_b32_e32 v26, v26, v73
	s_and_saveexec_b64 s[18:19], s[16:17]
	v_and_b32_e32 v27, 0x1fffc, v26
	v_mov_b32_e32 v37, 1
	ds_add_rtn_u32 v27, v27, v37 offset:5248
	s_or_b64 exec, exec, s[18:19]
	v_cmp_gt_i32_e64 s[18:19], s33, v25
	v_mov_b32_e32 v25, 0
	s_waitcnt vmcnt(2)
	v_lshrrev_b32_e32 v37, 14, v6
	v_and_b32_e32 v73, 0x1ffff, v6
	v_and_b32_e32 v37, 0x7f8, v37
	v_cmp_lt_u32_e64 s[48:49], s50, v73
	s_nop 1
	v_cndmask_b32_e64 v73, 0, 4, s[48:49]
	v_or_b32_e32 v37, v37, v73
	v_mov_b32_e32 v40, 0
	s_and_saveexec_b64 s[20:21], s[18:19]
	v_and_b32_e32 v39, 0x1fffc, v37
	v_mov_b32_e32 v40, 1
	ds_add_rtn_u32 v40, v39, v40 offset:5248
	s_or_b64 exec, exec, s[20:21]
	v_cmp_gt_i32_e64 s[20:21], s33, v24
	s_waitcnt vmcnt(1)
	v_lshrrev_b32_e32 v24, 14, v4
	v_and_b32_e32 v73, 0x1ffff, v4
	v_and_b32_e32 v24, 0x7f8, v24
	v_cmp_lt_u32_e64 s[48:49], s50, v73
	s_nop 1
	v_cndmask_b32_e64 v73, 0, 4, s[48:49]
	v_or_b32_e32 v24, v24, v73
	s_and_saveexec_b64 s[22:23], s[20:21]
	v_and_b32_e32 v25, 0x1fffc, v24
	v_mov_b32_e32 v39, 1
	ds_add_rtn_u32 v25, v25, v39 offset:5248
	s_or_b64 exec, exec, s[22:23]
	v_cmp_gt_i32_e64 s[22:23], s33, v21
	v_mov_b32_e32 v42, 0
	s_waitcnt vmcnt(0)
	v_lshrrev_b32_e32 v39, 14, v2
	v_and_b32_e32 v73, 0x1ffff, v2
	v_and_b32_e32 v39, 0x7f8, v39
	v_cmp_lt_u32_e64 s[48:49], s50, v73
	s_nop 1
	v_cndmask_b32_e64 v73, 0, 4, s[48:49]
	v_or_b32_e32 v39, v39, v73
	v_mov_b32_e32 v41, 0
	s_and_saveexec_b64 s[30:31], s[22:23]
	v_and_b32_e32 v21, 0x1fffc, v39
	v_mov_b32_e32 v41, 1
	ds_add_rtn_u32 v41, v21, v41 offset:5248
	s_or_b64 exec, exec, s[30:31]
	s_waitcnt lgkmcnt(0)
	s_barrier
	ds_read_b32 v42, v1 offset:5248
	v_lshlrev_b32_e32 v74, 2, v20
	s_waitcnt lgkmcnt(0)
	v_add_u32_dpp v21, v42, v42 row_shr:1 row_mask:0xf bank_mask:0xf bound_ctrl:1
	s_nop 1
	v_add_u32_dpp v21, v21, v21 row_shr:2 row_mask:0xf bank_mask:0xf bound_ctrl:1
	s_nop 1
	v_add_u32_dpp v21, v21, v21 row_shr:4 row_mask:0xf bank_mask:0xf bound_ctrl:1
	s_nop 1
	v_add_u32_dpp v43, v21, v21 row_shr:8 row_mask:0xf bank_mask:0xf bound_ctrl:1
	s_nop 1
	v_add_u32_dpp v43, v43, v43 row_bcast:15 row_mask:0xa bank_mask:0xf
	s_nop 1
	v_add_u32_dpp v43, v43, v43 row_bcast:31 row_mask:0xc bank_mask:0xf
	s_and_saveexec_b64 s[30:31], s[6:7]
	ds_write_b32 v74, v43 offset:4156
	s_or_b64 exec, exec, s[30:31]
	v_mov_b32_e32 v44, 0x103c
	s_waitcnt lgkmcnt(0)
	s_barrier
	ds_read2_b32 v[20:21], v44 offset1:1
	ds_read2_b32 v[46:47], v44 offset0:2 offset1:3
	ds_read2_b32 v[48:49], v44 offset0:4 offset1:5
	ds_read_b32 v50, v44 offset:24
	v_sub_u32_e32 v42, v43, v42
	s_waitcnt lgkmcnt(0)
	s_movk_i32 s51, 0x3f
	v_cmp_lt_u32_e64 s[48:49], s51, v0
	s_nop 1
	v_cndmask_b32_e64 v20, 0, v20, s[48:49]
	v_add_u32_e32 v42, v42, v20
	s_movk_i32 s51, 0x7f
	v_cmp_lt_u32_e64 s[48:49], s51, v0
	s_nop 1
	v_cndmask_b32_e64 v21, 0, v21, s[48:49]
	v_add_u32_e32 v42, v42, v21
	s_movk_i32 s51, 0xbf
	v_cmp_lt_u32_e64 s[48:49], s51, v0
	s_nop 1
	v_cndmask_b32_e64 v46, 0, v46, s[48:49]
	v_add_u32_e32 v42, v42, v46
	s_movk_i32 s51, 0xff
	v_cmp_lt_u32_e64 s[48:49], s51, v0
	s_nop 1
	v_cndmask_b32_e64 v47, 0, v47, s[48:49]
	v_add_u32_e32 v42, v42, v47
	s_movk_i32 s51, 0x13f
	v_cmp_lt_u32_e64 s[48:49], s51, v0
	s_nop 1
	v_cndmask_b32_e64 v48, 0, v48, s[48:49]
	v_add_u32_e32 v42, v42, v48
	s_movk_i32 s51, 0x17f
	v_cmp_lt_u32_e64 s[48:49], s51, v0
	s_nop 1
	v_cndmask_b32_e64 v49, 0, v49, s[48:49]
	v_add_u32_e32 v42, v42, v49
	s_movk_i32 s51, 0x1bf
	v_cmp_lt_u32_e64 s[48:49], s51, v0
	s_nop 1
	v_cndmask_b32_e64 v50, 0, v50, s[48:49]
	v_add_u32_e32 v42, v42, v50
	ds_write_b32 v1, v42 offset:5248
.LBB1_60:
	s_or_b64 exec, exec, s[6:7]
	s_waitcnt lgkmcnt(0)
	s_barrier
	v_and_b32_e32 v31, 0x1fffc, v31
	v_and_b32_e32 v30, 0x1fffc, v30
	v_and_b32_e32 v33, 0x1fffc, v33
	v_and_b32_e32 v32, 0x1fffc, v32
	v_and_b32_e32 v35, 0x1fffc, v35
	v_and_b32_e32 v26, 0x1fffc, v26
	v_and_b32_e32 v37, 0x1fffc, v37
	v_and_b32_e32 v24, 0x1fffc, v24
	v_and_b32_e32 v39, 0x1fffc, v39
	ds_read_b32 v31, v31 offset:5248
	ds_read_b32 v30, v30 offset:5248
	ds_read_b32 v33, v33 offset:5248
	ds_read_b32 v32, v32 offset:5248
	ds_read_b32 v35, v35 offset:5248
	ds_read_b32 v26, v26 offset:5248
	ds_read_b32 v37, v37 offset:5248
	ds_read_b32 v24, v24 offset:5248
	ds_read_b32 v39, v39 offset:5248
	v_lshlrev_b32_e32 v34, 3, v34
	v_lshlrev_b32_e32 v29, 3, v29
	v_lshlrev_b32_e32 v36, 3, v36
	v_lshlrev_b32_e32 v28, 3, v28
	v_lshlrev_b32_e32 v38, 3, v38
	v_lshlrev_b32_e32 v27, 3, v27
	v_lshlrev_b32_e32 v40, 3, v40
	v_lshlrev_b32_e32 v25, 3, v25
	v_lshlrev_b32_e32 v41, 3, v41
	v_and_b32_e32 v18, 0x1ffff, v18
	v_and_b32_e32 v16, 0x1ffff, v16
	v_and_b32_e32 v12, 0x1ffff, v12
	v_and_b32_e32 v8, 0x1ffff, v8
	v_and_b32_e32 v14, 0x1ffff, v14
	v_and_b32_e32 v10, 0x1ffff, v10
	v_and_b32_e32 v6, 0x1ffff, v6
	v_and_b32_e32 v4, 0x1ffff, v4
	v_and_b32_e32 v2, 0x1ffff, v2
	s_mov_b64 s[4:5], exec
	s_waitcnt lgkmcnt(8)
	s_and_b64 exec, exec, vcc
	v_lshl_add_u32 v31, v31, 3, v34
	ds_write_b64 v31, v[18:19] offset:8192
	s_waitcnt lgkmcnt(7)
	s_and_b64 exec, exec, s[8:9]
	v_lshl_add_u32 v30, v30, 3, v29
	ds_write_b64 v30, v[16:17] offset:8192
	s_waitcnt lgkmcnt(6)
	s_and_b64 exec, exec, s[10:11]
	v_lshl_add_u32 v33, v33, 3, v36
	ds_write_b64 v33, v[12:13] offset:8192
	s_waitcnt lgkmcnt(5)
	s_and_b64 exec, exec, s[12:13]
	v_lshl_add_u32 v32, v32, 3, v28
	ds_write_b64 v32, v[8:9] offset:8192
	s_waitcnt lgkmcnt(4)
	s_and_b64 exec, exec, s[14:15]
	v_lshl_add_u32 v35, v35, 3, v38
	ds_write_b64 v35, v[14:15] offset:8192
	s_waitcnt lgkmcnt(3)
	s_and_b64 exec, exec, s[16:17]
	v_lshl_add_u32 v26, v26, 3, v27
	ds_write_b64 v26, v[10:11] offset:8192
	s_waitcnt lgkmcnt(2)
	s_and_b64 exec, exec, s[18:19]
	v_lshl_add_u32 v37, v37, 3, v40
	ds_write_b64 v37, v[6:7] offset:8192
	s_waitcnt lgkmcnt(1)
	s_and_b64 exec, exec, s[20:21]
	v_lshl_add_u32 v24, v24, 3, v25
	ds_write_b64 v24, v[4:5] offset:8192
	s_waitcnt lgkmcnt(0)
	s_and_b64 exec, exec, s[22:23]
	v_lshl_add_u32 v39, v39, 3, v41
	ds_write_b64 v39, v[2:3] offset:8192
.LBB1_70:
	s_or_b64 exec, exec, s[4:5]
	v_lshrrev_b32_e32 v7, 1, v0
	v_lshlrev_b32_e32 v1, 2, v7
	s_waitcnt lgkmcnt(0)
	s_barrier
	v_lshlrev_b32_e32 v73, 3, v7
	ds_read_b32 v6, v73 offset:5248
	s_movk_i32 s4, 0x1fe
	v_cmp_gt_u32_e64 s[4:5], s4, v0
	v_mov_b32_e32 v9, s33
	s_and_saveexec_b64 s[6:7], s[4:5]
	ds_read_b32 v9, v73 offset:5256
	s_or_b64 exec, exec, s[6:7]
	v_and_b32_e32 v8, 1, v0
	s_waitcnt lgkmcnt(0)
	v_add_u32_e32 v10, v6, v8
	v_add_u32_e32 v2, 6, v10
	v_mov_b32_e32 v5, 0
	v_cmp_lt_i32_e64 s[4:5], v2, v9
	v_mov_b32_e32 v4, v5
	v_mov_b32_e32 v3, v5
	v_mov_b32_e32 v2, v5
	s_and_saveexec_b64 s[6:7], s[4:5]
	s_cbranch_execz .LBB1_76
	v_mov_b32_e32 v2, 0x2004
	v_lshl_add_u32 v11, v10, 3, v2
	v_mov_b32_e32 v2, 0
	s_mov_b64 s[8:9], 0
	v_mov_b32_e32 v3, v2
	v_mov_b32_e32 v4, v2
	v_mov_b32_e32 v5, v2
